# MLA loop first-half step: exp2/fp8-pack of the current half tile moved into the shadow of the three QK MFMAs (temps v224-239), on top of the static priority for waves 4-7
# baseline (speedup 1.0000x reference)
.LBB0_570:
	s_waitcnt lgkmcnt(4)
	v_mfma_scale_f32_32x32x64_f8f6f4 v[80:95], v[80:87], v[120:127], 0, v205, v205 op_sel_hi:[0,0,0]
	v_exp_f32_e32 v224, v178
	v_exp_f32_e32 v225, v179
	v_exp_f32_e32 v226, v176
	v_exp_f32_e32 v227, v177
	v_exp_f32_e32 v228, v162
	v_exp_f32_e32 v229, v163
	v_exp_f32_e32 v230, v160
	v_exp_f32_e32 v231, v161
	s_mov_b64 s[4:5], exec
	s_cmp_ge_u32 s18, s20
	s_waitcnt lgkmcnt(2)
	v_mfma_scale_f32_32x32x64_f8f6f4 v[80:95], v[104:111], v[128:135], v[80:95], v205, v205 op_sel_hi:[0,0,0]
	v_exp_f32_e32 v232, v158
	v_exp_f32_e32 v233, v159
	v_exp_f32_e32 v234, v156
	v_exp_f32_e32 v235, v157
	v_exp_f32_e32 v236, v154
	v_exp_f32_e32 v237, v155
	v_exp_f32_e32 v238, v152
	v_exp_f32_e32 v239, v153
	s_waitcnt lgkmcnt(0)
	v_mfma_scale_f32_32x32x64_f8f6f4 v[80:95], v[96:103], v[136:143], v[80:95], v205, v205 op_sel_hi:[0,0,0]
	v_mov_b32_e32 v144, 0
	v_mov_b32_e32 v145, 0
	v_mov_b32_e32 v146, 0
	v_mov_b32_e32 v147, 0
	v_cvt_pk_fp8_f32 v144, v224, v225
	v_cvt_pk_fp8_f32 v145, v228, v229
	v_cvt_pk_fp8_f32 v146, v232, v233
	v_cvt_pk_fp8_f32 v147, v236, v237
	v_cvt_pk_fp8_f32 v144, v226, v227 op_sel:[0,0,1]
	v_cvt_pk_fp8_f32 v145, v230, v231 op_sel:[0,0,1]
	v_cvt_pk_fp8_f32 v146, v234, v235 op_sel:[0,0,1]
	v_cvt_pk_fp8_f32 v147, v238, v239 op_sel:[0,0,1]
	s_nop 7
	v_max_f32_e32 v96, v81, v81
	v_max_f32_e32 v97, v80, v80
	v_max_f32_e32 v96, v97, v96
	v_max3_f32 v96, v96, v82, v83
	v_max3_f32 v96, v96, v84, v85
	v_max3_f32 v96, v96, v86, v87
	v_max3_f32 v96, v96, v88, v89
	v_max3_f32 v96, v96, v90, v91
	v_max3_f32 v96, v96, v92, v93
	v_max3_f32 v96, v96, v94, v95
	v_mov_b32_e32 v97, v96
	s_nop 1
	v_permlane32_swap_b32_e32 v96, v97
	v_max_f32_e32 v97, v97, v97
	v_max_f32_e32 v96, v96, v96
	v_max_f32_e32 v96, v96, v97
	v_fma_f32 v97, v96, s40, -v192
	v_cmp_ge_f32_e32 vcc, s70, v97
	s_cbranch_scc1 .LBB0_577
	s_xor_b32 s25, s23, 1
	s_lshl_b32 s18, s25, 15
	s_add_i32 s26, s18, 0
	v_add3_u32 v97, s26, v212, v190
	s_waitcnt vmcnt(1)
	ds_write_b128 v97, v[168:171]
	s_and_saveexec_b64 s[18:19], s[0:1]
	v_add3_u32 v97, s26, v215, v188
	ds_write_b128 v97, v[164:167]
	s_or_b64 exec, exec, s[18:19]
	v_lshl_add_u32 v97, s25, 14, v207
	s_cmp_ge_u32 s78, s74
	s_waitcnt vmcnt(0)
	ds_write_b128 v97, v[172:175]
	s_cbranch_scc1 .LBB0_577
	s_cmp_lt_u32 s78, s77
	s_cselect_b32 s18, 0, s77
	s_cselect_b32 s19, s76, s75
	s_lshl_b32 s18, s18, 6
	s_sub_i32 s25, s19, s18
	s_add_i32 s25, s25, s22
	v_add_u32_e32 v97, s25, v210
	v_mad_i64_i32 v[98:99], s[18:19], v97, s64, v[194:195]
	global_load_dwordx4 v[168:171], v[98:99], off
	s_and_saveexec_b64 s[18:19], s[0:1]
	s_cbranch_execz .LBB0_576
	v_add_u32_e32 v97, s25, v213
	v_mad_i64_i32 v[98:99], s[26:27], v97, s64, v[196:197]
	global_load_dwordx4 v[164:167], v[98:99], off

.LBB0_577:
	v_mul_f32_e32 v96, 0x3dd53b94, v96
	v_add_f32_e32 v96, 0xc0a00000, v96
	v_max_f32_e32 v97, v192, v192
	v_max_f32_e32 v189, v97, v96
	v_sub_f32_e32 v96, v192, v189
	v_exp_f32_e32 v96, v96
	s_cmp_eq_u64 vcc, s[4:5]
	s_cselect_b64 s[4:5], -1, 0
	v_cndmask_b32_e64 v191, v96, 1.0, s[4:5]
	s_xor_b32 s18, s24, 0x8000
	v_add_u32_e32 v105, s18, v216
	s_waitcnt lgkmcnt(0)
	s_barrier
	ds_read_b128 v[96:99], v105
	ds_read_b128 v[100:103], v105 offset:16
	ds_read_b128 v[156:159], v105 offset:64
	ds_read_b128 v[160:163], v105 offset:80
	v_add_u32_e32 v105, v105, v217
	ds_read_b128 v[148:151], v105 offset:128
	ds_read_b128 v[152:155], v105 offset:160
	v_cmp_gt_f32_e32 vcc, 1.0, v191
	s_cbranch_vccz .LBB0_565
	s_and_saveexec_b64 s[18:19], s[2:3]
	s_cbranch_execz .LBB0_564
	ds_write_b32 v209, v191 offset:128
	s_branch .LBB0_564

.LBB0_1880:
	s_waitcnt lgkmcnt(4)
	v_mfma_scale_f32_32x32x64_f8f6f4 v[80:95], v[80:87], v[120:127], 0, v207, v207 op_sel_hi:[0,0,0]
	v_exp_f32_e32 v224, v178
	v_exp_f32_e32 v225, v179
	v_exp_f32_e32 v226, v176
	v_exp_f32_e32 v227, v177
	v_exp_f32_e32 v228, v162
	v_exp_f32_e32 v229, v163
	v_exp_f32_e32 v230, v160
	v_exp_f32_e32 v231, v161
	s_xor_b32 s22, s24, 1
	s_lshl_b32 s18, s22, 15
	s_add_i32 s23, s18, 0
	s_mov_b64 s[20:21], exec
	s_waitcnt lgkmcnt(2)
	v_mfma_scale_f32_32x32x64_f8f6f4 v[80:95], v[104:111], v[128:135], v[80:95], v207, v207 op_sel_hi:[0,0,0]
	v_exp_f32_e32 v232, v158
	v_exp_f32_e32 v233, v159
	v_exp_f32_e32 v234, v156
	v_exp_f32_e32 v235, v157
	v_exp_f32_e32 v236, v154
	v_exp_f32_e32 v237, v155
	v_exp_f32_e32 v238, v152
	v_exp_f32_e32 v239, v153
	s_waitcnt lgkmcnt(0)
	v_mfma_scale_f32_32x32x64_f8f6f4 v[80:95], v[96:103], v[136:143], v[80:95], v207, v207 op_sel_hi:[0,0,0]
	v_mov_b32_e32 v144, 0
	v_mov_b32_e32 v145, 0
	v_mov_b32_e32 v146, 0
	v_mov_b32_e32 v147, 0
	v_cvt_pk_fp8_f32 v144, v224, v225
	v_cvt_pk_fp8_f32 v145, v228, v229
	v_cvt_pk_fp8_f32 v146, v232, v233
	v_cvt_pk_fp8_f32 v147, v236, v237
	v_cvt_pk_fp8_f32 v144, v226, v227 op_sel:[0,0,1]
	v_cvt_pk_fp8_f32 v145, v230, v231 op_sel:[0,0,1]
	v_cvt_pk_fp8_f32 v146, v234, v235 op_sel:[0,0,1]
	v_cvt_pk_fp8_f32 v147, v238, v239 op_sel:[0,0,1]
	s_nop 7
	v_max_f32_e32 v96, v81, v81
	v_max_f32_e32 v97, v80, v80
	v_max_f32_e32 v96, v97, v96
	v_max3_f32 v96, v96, v82, v83
	v_max3_f32 v96, v96, v84, v85
	v_max3_f32 v96, v96, v86, v87
	v_max3_f32 v96, v96, v88, v89
	v_max3_f32 v96, v96, v90, v91
	v_max3_f32 v96, v96, v92, v93
	v_max3_f32 v96, v96, v94, v95
	v_mov_b32_e32 v97, v96
	s_nop 1
	v_permlane32_swap_b32_e32 v96, v97
	v_max_f32_e32 v97, v97, v97
	v_max_f32_e32 v96, v96, v96
	v_max_f32_e32 v96, v96, v97
	v_fma_f32 v97, v96, s38, -v194
	v_cmp_ge_f32_e64 s[4:5], s68, v97
	v_add3_u32 v97, s23, v210, v190
	s_waitcnt vmcnt(1)
	ds_write_b128 v97, v[168:171]
	s_and_saveexec_b64 s[18:19], s[0:1]
	v_add3_u32 v97, s23, v216, v192
	ds_write_b128 v97, v[164:167]
	s_or_b64 exec, exec, s[18:19]
	s_cmpk_gt_u32 s17, 0x83
	s_cselect_b64 s[18:19], -1, 0
	v_lshl_add_u32 v97, s22, 14, v211
	s_and_b64 vcc, exec, s[18:19]
	s_waitcnt vmcnt(0)
	ds_write_b128 v97, v[172:175]
	s_cbranch_vccnz .LBB0_1886
	s_cmpk_lt_u32 s17, 0x7c
	s_cselect_b32 s22, 0, 0xffffffc0
	s_cselect_b32 s23, s74, s75
	s_add_i32 s22, s22, s76
	s_lshl_b32 s26, s22, 6
	s_add_i32 s26, s26, s23
	v_add_u32_e32 v97, s26, v189
	v_mad_i64_i32 v[98:99], s[22:23], v97, s62, v[196:197]
	global_load_dwordx4 v[168:171], v[98:99], off
	s_and_saveexec_b64 s[22:23], s[0:1]
	s_cbranch_execz .LBB0_1885
	v_add_u32_e32 v97, s26, v212
	v_mad_i64_i32 v[98:99], s[28:29], v97, s62, v[198:199]
	global_load_dwordx4 v[164:167], v[98:99], off

.LBB0_1886:
	v_mul_f32_e32 v96, 0x3dd53b94, v96
	v_add_f32_e32 v96, 0xc0a00000, v96
	v_max_f32_e32 v97, v194, v194
	v_max_f32_e32 v191, v97, v96
	v_sub_f32_e32 v96, v194, v191
	v_exp_f32_e32 v96, v96
	s_cmp_eq_u64 s[4:5], s[20:21]
	s_cselect_b64 s[4:5], -1, 0
	v_cndmask_b32_e64 v193, v96, 1.0, s[4:5]
	s_xor_b32 s20, s25, 0x8000
	v_add_u32_e32 v105, s20, v214
	s_waitcnt lgkmcnt(0)
	s_barrier
	ds_read_b128 v[96:99], v105
	ds_read_b128 v[100:103], v105 offset:16
	ds_read_b128 v[156:159], v105 offset:64
	ds_read_b128 v[160:163], v105 offset:80
	v_add_u32_e32 v105, v105, v215
	ds_read_b128 v[148:151], v105 offset:128
	ds_read_b128 v[152:155], v105 offset:160
	v_cmp_gt_f32_e32 vcc, 1.0, v193
	s_cbranch_vccz .LBB0_1875
	s_and_saveexec_b64 s[20:21], s[2:3]
	s_cbranch_execz .LBB0_1874
	ds_write_b32 v208, v193 offset:128
	s_branch .LBB0_1874
